# v69 + early leading-half epilogue for the in-proj GEMM (ALIGN barrier moved after the 2nd store, scc-based)
# baseline (speedup 1.0000x reference)
.LBB0_287:
	ds_read_b128 v[134:137], v198
	ds_read_b128 v[138:141], v198 offset:1024
	ds_read_b128 v[142:145], v198 offset:2048
	ds_read_b128 v[146:149], v198 offset:3072
	ds_read_b128 v[150:153], v199
	ds_read_b128 v[154:157], v199 offset:1024
	ds_read_b128 v[158:161], v199 offset:2048
	ds_read_b128 v[178:181], v199 offset:3072
	s_add_u32 s14, s30, 0xfffc0080
	s_addc_u32 s22, s31, -1
	s_cmp_eq_u32 s70, 12
	s_cselect_b32 s37, s54, s22
	s_cselect_b32 s36, s55, s14
	s_cselect_b32 s23, s56, s69
	s_cselect_b32 s22, s57, s68
	s_mov_b32 m0, s58
	v_lshl_add_u64 v[162:163], s[30:31], 0, v[170:171]
	ds_read_b128 v[182:185], v197
	ds_read_b128 v[190:193], v197 offset:1024
	ds_read_b128 v[200:203], v197 offset:2048
	ds_read_b128 v[204:207], v197 offset:3072
	ds_read_b128 v[208:211], v197 offset:4096
	ds_read_b128 v[212:215], v197 offset:5120
	ds_read_b128 v[216:219], v197 offset:6144
	ds_read_b128 v[222:225], v197 offset:7168
	global_load_lds_dwordx4 v[162:163], off
	v_lshl_add_u64 v[162:163], s[30:31], 0, v[172:173]
	s_mov_b32 m0, s59
	s_nop 0
	global_load_lds_dwordx4 v[162:163], off
	s_waitcnt vmcnt(8)
	s_waitcnt lgkmcnt(0)
	s_barrier
	v_mfma_f32_16x16x32_bf16 v[128:131], v[134:137], v[182:185], v[128:131]
	s_setprio 1
	v_mfma_f32_16x16x32_bf16 v[124:127], v[142:145], v[182:185], v[124:127]
	v_mfma_f32_16x16x32_bf16 v[116:119], v[142:145], v[200:203], v[116:119]
	v_mfma_f32_16x16x32_bf16 v[120:123], v[134:137], v[200:203], v[120:123]
	v_mfma_f32_16x16x32_bf16 v[112:115], v[134:137], v[208:211], v[112:115]
	v_mfma_f32_16x16x32_bf16 v[108:111], v[142:145], v[208:211], v[108:111]
	v_mfma_f32_16x16x32_bf16 v[100:103], v[142:145], v[216:219], v[100:103]
	v_mfma_f32_16x16x32_bf16 v[104:107], v[134:137], v[216:219], v[104:107]
	v_mfma_f32_16x16x32_bf16 v[128:131], v[138:141], v[190:193], v[128:131]
	v_mfma_f32_16x16x32_bf16 v[124:127], v[146:149], v[190:193], v[124:127]
	v_mfma_f32_16x16x32_bf16 v[116:119], v[146:149], v[204:207], v[116:119]
	v_mfma_f32_16x16x32_bf16 v[120:123], v[138:141], v[204:207], v[120:123]
	v_mfma_f32_16x16x32_bf16 v[112:115], v[138:141], v[212:215], v[112:115]
	v_mfma_f32_16x16x32_bf16 v[108:111], v[146:149], v[212:215], v[108:111]
	v_mfma_f32_16x16x32_bf16 v[100:103], v[146:149], v[222:225], v[100:103]
	v_mfma_f32_16x16x32_bf16 v[104:107], v[138:141], v[222:225], v[104:107]
	s_setprio 0
	s_setprio 1
	v_mfma_f32_16x16x32_bf16 v[96:99], v[150:153], v[182:185], v[96:99]
	v_mfma_f32_16x16x32_bf16 v[92:95], v[158:161], v[182:185], v[92:95]
	v_mfma_f32_16x16x32_bf16 v[84:87], v[158:161], v[200:203], v[84:87]
	v_mfma_f32_16x16x32_bf16 v[88:91], v[150:153], v[200:203], v[88:91]
	v_mfma_f32_16x16x32_bf16 v[80:83], v[150:153], v[208:211], v[80:83]
	v_mfma_f32_16x16x32_bf16 v[76:79], v[158:161], v[208:211], v[76:79]
	v_mfma_f32_16x16x32_bf16 v[68:71], v[158:161], v[216:219], v[68:71]
	v_mfma_f32_16x16x32_bf16 v[72:75], v[150:153], v[216:219], v[72:75]
	v_mfma_f32_16x16x32_bf16 v[96:99], v[154:157], v[190:193], v[96:99]
	v_mfma_f32_16x16x32_bf16 v[92:95], v[178:181], v[190:193], v[92:95]
	v_mfma_f32_16x16x32_bf16 v[84:87], v[178:181], v[204:207], v[84:87]
	v_mfma_f32_16x16x32_bf16 v[88:91], v[154:157], v[204:207], v[88:91]
	v_mfma_f32_16x16x32_bf16 v[80:83], v[154:157], v[212:215], v[80:83]
	v_mfma_f32_16x16x32_bf16 v[76:79], v[178:181], v[212:215], v[76:79]
	v_mfma_f32_16x16x32_bf16 v[68:71], v[178:181], v[222:225], v[68:71]
	s_barrier
	v_mfma_f32_16x16x32_bf16 v[72:75], v[154:157], v[222:225], v[72:75]
	s_setprio 0
	s_mov_b32 m0, s60
	v_lshl_add_u64 v[162:163], s[22:23], 0, v[34:35]
	s_add_u32 s72, s22, 0x40000
	ds_read_b128 v[182:185], v197 offset:16384
	ds_read_b128 v[190:193], v197 offset:17408
	ds_read_b128 v[200:203], v197 offset:18432
	ds_read_b128 v[204:207], v197 offset:19456
	ds_read_b128 v[208:211], v197 offset:20480
	ds_read_b128 v[212:215], v197 offset:21504
	ds_read_b128 v[216:219], v197 offset:22528
	ds_read_b128 v[222:225], v197 offset:23552
	global_load_lds_dwordx4 v[162:163], off
	v_lshl_add_u64 v[174:175], s[22:23], 0, v[164:165]
	s_mov_b32 m0, s61
	s_addc_u32 s73, s23, 0
	global_load_lds_dwordx4 v[174:175], off
	v_lshl_add_u64 v[194:195], s[72:73], 0, v[34:35]
	s_mov_b32 m0, s62
	v_lshl_add_u64 v[226:227], s[36:37], 0, v[166:167]
	global_load_lds_dwordx4 v[194:195], off
	v_lshl_add_u64 v[194:195], s[72:73], 0, v[164:165]
	s_mov_b32 m0, s63
	s_nop 0
	global_load_lds_dwordx4 v[194:195], off
	v_lshl_add_u64 v[194:195], s[36:37], 0, v[168:169]
	s_mov_b32 m0, s41
	s_nop 0
	global_load_lds_dwordx4 v[194:195], off
	s_mov_b32 m0, s42
	s_nop 0
	global_load_lds_dwordx4 v[226:227], off
	s_waitcnt vmcnt(8)
	s_waitcnt lgkmcnt(0)
	s_barrier
	v_mfma_f32_16x16x32_bf16 v[64:67], v[134:137], v[182:185], v[64:67]
	s_setprio 1
	v_mfma_f32_16x16x32_bf16 v[60:63], v[142:145], v[182:185], v[60:63]
	v_mfma_f32_16x16x32_bf16 v[52:55], v[142:145], v[200:203], v[52:55]
	v_mfma_f32_16x16x32_bf16 v[56:59], v[134:137], v[200:203], v[56:59]
	v_mfma_f32_16x16x32_bf16 v[48:51], v[134:137], v[208:211], v[48:51]
	v_mfma_f32_16x16x32_bf16 v[44:47], v[142:145], v[208:211], v[44:47]
	v_mfma_f32_16x16x32_bf16 v[36:39], v[142:145], v[216:219], v[36:39]
	v_mfma_f32_16x16x32_bf16 v[40:43], v[134:137], v[216:219], v[40:43]
	v_mfma_f32_16x16x32_bf16 v[64:67], v[138:141], v[190:193], v[64:67]
	v_mfma_f32_16x16x32_bf16 v[60:63], v[146:149], v[190:193], v[60:63]
	v_mfma_f32_16x16x32_bf16 v[52:55], v[146:149], v[204:207], v[52:55]
	v_mfma_f32_16x16x32_bf16 v[56:59], v[138:141], v[204:207], v[56:59]
	v_mfma_f32_16x16x32_bf16 v[48:51], v[138:141], v[212:215], v[48:51]
	v_mfma_f32_16x16x32_bf16 v[44:47], v[146:149], v[212:215], v[44:47]
	v_mfma_f32_16x16x32_bf16 v[36:39], v[146:149], v[222:225], v[36:39]
	v_mfma_f32_16x16x32_bf16 v[40:43], v[138:141], v[222:225], v[40:43]
	s_setprio 0
	s_setprio 1
	v_mfma_f32_16x16x32_bf16 v[30:33], v[150:153], v[182:185], v[30:33]
	v_mfma_f32_16x16x32_bf16 v[26:29], v[158:161], v[182:185], v[26:29]
	v_mfma_f32_16x16x32_bf16 v[18:21], v[158:161], v[200:203], v[18:21]
	v_mfma_f32_16x16x32_bf16 v[22:25], v[150:153], v[200:203], v[22:25]
	v_mfma_f32_16x16x32_bf16 v[14:17], v[150:153], v[208:211], v[14:17]
	v_mfma_f32_16x16x32_bf16 v[10:13], v[158:161], v[208:211], v[10:13]
	v_mfma_f32_16x16x32_bf16 v[2:5], v[158:161], v[216:219], v[2:5]
	v_mfma_f32_16x16x32_bf16 v[6:9], v[150:153], v[216:219], v[6:9]
	v_mfma_f32_16x16x32_bf16 v[30:33], v[154:157], v[190:193], v[30:33]
	v_mfma_f32_16x16x32_bf16 v[26:29], v[178:181], v[190:193], v[26:29]
	v_mfma_f32_16x16x32_bf16 v[18:21], v[178:181], v[204:207], v[18:21]
	v_mfma_f32_16x16x32_bf16 v[22:25], v[154:157], v[204:207], v[22:25]
	v_mfma_f32_16x16x32_bf16 v[14:17], v[154:157], v[212:215], v[14:17]
	v_mfma_f32_16x16x32_bf16 v[10:13], v[178:181], v[212:215], v[10:13]
	v_mfma_f32_16x16x32_bf16 v[2:5], v[178:181], v[222:225], v[2:5]
	s_barrier
	v_mfma_f32_16x16x32_bf16 v[6:9], v[154:157], v[222:225], v[6:9]
	s_setprio 0
	ds_read_b128 v[134:137], v132
	ds_read_b128 v[138:141], v132 offset:1024
	ds_read_b128 v[142:145], v132 offset:2048
	ds_read_b128 v[146:149], v132 offset:3072
	ds_read_b128 v[150:153], v133
	ds_read_b128 v[154:157], v133 offset:1024
	ds_read_b128 v[158:161], v133 offset:2048
	ds_read_b128 v[178:181], v133 offset:3072
	s_add_u32 s36, s36, 0x40000
	s_addc_u32 s37, s37, 0
	s_mov_b32 m0, s43
	v_lshl_add_u64 v[228:229], s[36:37], 0, v[168:169]
	ds_read_b128 v[182:185], v197 offset:32768
	ds_read_b128 v[190:193], v197 offset:33792
	ds_read_b128 v[200:203], v197 offset:34816
	ds_read_b128 v[204:207], v197 offset:35840
	ds_read_b128 v[208:211], v197 offset:36864
	ds_read_b128 v[212:215], v197 offset:37888
	ds_read_b128 v[216:219], v197 offset:38912
	ds_read_b128 v[222:225], v197 offset:39936
	global_load_lds_dwordx4 v[228:229], off
	v_lshl_add_u64 v[228:229], s[36:37], 0, v[166:167]
	s_mov_b32 m0, s44
	s_nop 0
	global_load_lds_dwordx4 v[228:229], off
	s_waitcnt vmcnt(8)
	s_waitcnt lgkmcnt(0)
	s_barrier
	v_mfma_f32_16x16x32_bf16 v[128:131], v[134:137], v[182:185], v[128:131]
	s_setprio 1
	v_mfma_f32_16x16x32_bf16 v[124:127], v[142:145], v[182:185], v[124:127]
	v_mfma_f32_16x16x32_bf16 v[116:119], v[142:145], v[200:203], v[116:119]
	v_mfma_f32_16x16x32_bf16 v[120:123], v[134:137], v[200:203], v[120:123]
	v_mfma_f32_16x16x32_bf16 v[112:115], v[134:137], v[208:211], v[112:115]
	v_mfma_f32_16x16x32_bf16 v[108:111], v[142:145], v[208:211], v[108:111]
	v_mfma_f32_16x16x32_bf16 v[100:103], v[142:145], v[216:219], v[100:103]
	v_mfma_f32_16x16x32_bf16 v[104:107], v[134:137], v[216:219], v[104:107]
	v_mfma_f32_16x16x32_bf16 v[128:131], v[138:141], v[190:193], v[128:131]
	v_mfma_f32_16x16x32_bf16 v[124:127], v[146:149], v[190:193], v[124:127]
	v_mfma_f32_16x16x32_bf16 v[116:119], v[146:149], v[204:207], v[116:119]
	v_mfma_f32_16x16x32_bf16 v[120:123], v[138:141], v[204:207], v[120:123]
	v_mfma_f32_16x16x32_bf16 v[112:115], v[138:141], v[212:215], v[112:115]
	v_mfma_f32_16x16x32_bf16 v[108:111], v[146:149], v[212:215], v[108:111]
	v_mfma_f32_16x16x32_bf16 v[100:103], v[146:149], v[222:225], v[100:103]
	v_mfma_f32_16x16x32_bf16 v[104:107], v[138:141], v[222:225], v[104:107]
	s_setprio 0
	s_setprio 1
	v_mfma_f32_16x16x32_bf16 v[96:99], v[150:153], v[182:185], v[96:99]
	v_mfma_f32_16x16x32_bf16 v[92:95], v[158:161], v[182:185], v[92:95]
	v_mfma_f32_16x16x32_bf16 v[84:87], v[158:161], v[200:203], v[84:87]
	v_mfma_f32_16x16x32_bf16 v[88:91], v[150:153], v[200:203], v[88:91]
	v_mfma_f32_16x16x32_bf16 v[80:83], v[150:153], v[208:211], v[80:83]
	v_mfma_f32_16x16x32_bf16 v[76:79], v[158:161], v[208:211], v[76:79]
	v_mfma_f32_16x16x32_bf16 v[68:71], v[158:161], v[216:219], v[68:71]
	v_mfma_f32_16x16x32_bf16 v[72:75], v[150:153], v[216:219], v[72:75]
	v_mfma_f32_16x16x32_bf16 v[96:99], v[154:157], v[190:193], v[96:99]
	v_mfma_f32_16x16x32_bf16 v[92:95], v[178:181], v[190:193], v[92:95]
	v_mfma_f32_16x16x32_bf16 v[84:87], v[178:181], v[204:207], v[84:87]
	v_mfma_f32_16x16x32_bf16 v[88:91], v[154:157], v[204:207], v[88:91]
	v_mfma_f32_16x16x32_bf16 v[80:83], v[154:157], v[212:215], v[80:83]
	v_mfma_f32_16x16x32_bf16 v[76:79], v[178:181], v[212:215], v[76:79]
	v_mfma_f32_16x16x32_bf16 v[68:71], v[178:181], v[222:225], v[68:71]
	s_barrier
	v_mfma_f32_16x16x32_bf16 v[72:75], v[154:157], v[222:225], v[72:75]
	s_setprio 0
	s_mov_b32 m0, s64
	v_lshl_add_u64 v[162:163], v[162:163], 0, s[18:19]
	s_add_u32 s22, s22, 0x40080
	ds_read_b128 v[182:185], v197 offset:49152
	ds_read_b128 v[190:193], v197 offset:50176
	ds_read_b128 v[200:203], v197 offset:51200
	ds_read_b128 v[204:207], v197 offset:52224
	ds_read_b128 v[208:211], v197 offset:53248
	ds_read_b128 v[212:215], v197 offset:54272
	ds_read_b128 v[216:219], v197 offset:55296
	ds_read_b128 v[222:225], v197 offset:56320
	global_load_lds_dwordx4 v[162:163], off
	v_lshl_add_u64 v[162:163], v[174:175], 0, s[18:19]
	s_mov_b32 m0, s65
	s_addc_u32 s23, s23, 0
	global_load_lds_dwordx4 v[162:163], off
	v_lshl_add_u64 v[162:163], s[22:23], 0, v[34:35]
	s_mov_b32 m0, s66
	s_nop 0
	global_load_lds_dwordx4 v[162:163], off
	v_lshl_add_u64 v[162:163], s[22:23], 0, v[164:165]
	s_mov_b32 m0, s67
	s_nop 0
	global_load_lds_dwordx4 v[162:163], off
	v_lshl_add_u64 v[162:163], v[194:195], 0, s[18:19]
	s_mov_b32 m0, s47
	s_nop 0
	global_load_lds_dwordx4 v[162:163], off
	v_lshl_add_u64 v[162:163], v[226:227], 0, s[18:19]
	s_mov_b32 m0, s48
	s_nop 0
	global_load_lds_dwordx4 v[162:163], off
	s_waitcnt vmcnt(8)
	s_waitcnt lgkmcnt(0)
	s_barrier
	v_mfma_f32_16x16x32_bf16 v[64:67], v[134:137], v[182:185], v[64:67]
	s_setprio 1
	v_mfma_f32_16x16x32_bf16 v[60:63], v[142:145], v[182:185], v[60:63]
	v_mfma_f32_16x16x32_bf16 v[52:55], v[142:145], v[200:203], v[52:55]
	v_mfma_f32_16x16x32_bf16 v[56:59], v[134:137], v[200:203], v[56:59]
	v_mfma_f32_16x16x32_bf16 v[48:51], v[134:137], v[208:211], v[48:51]
	v_mfma_f32_16x16x32_bf16 v[44:47], v[142:145], v[208:211], v[44:47]
	v_mfma_f32_16x16x32_bf16 v[36:39], v[142:145], v[216:219], v[36:39]
	v_mfma_f32_16x16x32_bf16 v[40:43], v[134:137], v[216:219], v[40:43]
	v_mfma_f32_16x16x32_bf16 v[64:67], v[138:141], v[190:193], v[64:67]
	v_mfma_f32_16x16x32_bf16 v[60:63], v[146:149], v[190:193], v[60:63]
	v_mfma_f32_16x16x32_bf16 v[52:55], v[146:149], v[204:207], v[52:55]
	v_mfma_f32_16x16x32_bf16 v[56:59], v[138:141], v[204:207], v[56:59]
	v_mfma_f32_16x16x32_bf16 v[48:51], v[138:141], v[212:215], v[48:51]
	v_mfma_f32_16x16x32_bf16 v[44:47], v[146:149], v[212:215], v[44:47]
	v_mfma_f32_16x16x32_bf16 v[36:39], v[146:149], v[222:225], v[36:39]
	v_mfma_f32_16x16x32_bf16 v[40:43], v[138:141], v[222:225], v[40:43]
	s_setprio 0
	s_setprio 1
	v_mfma_f32_16x16x32_bf16 v[30:33], v[150:153], v[182:185], v[30:33]
	v_mfma_f32_16x16x32_bf16 v[26:29], v[158:161], v[182:185], v[26:29]
	v_mfma_f32_16x16x32_bf16 v[18:21], v[158:161], v[200:203], v[18:21]
	v_mfma_f32_16x16x32_bf16 v[22:25], v[150:153], v[200:203], v[22:25]
	v_mfma_f32_16x16x32_bf16 v[14:17], v[150:153], v[208:211], v[14:17]
	v_mfma_f32_16x16x32_bf16 v[10:13], v[158:161], v[208:211], v[10:13]
	v_mfma_f32_16x16x32_bf16 v[2:5], v[158:161], v[216:219], v[2:5]
	v_mfma_f32_16x16x32_bf16 v[6:9], v[150:153], v[216:219], v[6:9]
	v_mfma_f32_16x16x32_bf16 v[30:33], v[154:157], v[190:193], v[30:33]
	v_mfma_f32_16x16x32_bf16 v[26:29], v[178:181], v[190:193], v[26:29]
	v_mfma_f32_16x16x32_bf16 v[18:21], v[178:181], v[204:207], v[18:21]
	v_mfma_f32_16x16x32_bf16 v[22:25], v[154:157], v[204:207], v[22:25]
	v_mfma_f32_16x16x32_bf16 v[14:17], v[154:157], v[212:215], v[14:17]
	v_mfma_f32_16x16x32_bf16 v[10:13], v[178:181], v[212:215], v[10:13]
	v_mfma_f32_16x16x32_bf16 v[2:5], v[178:181], v[222:225], v[2:5]
	s_barrier
	v_mfma_f32_16x16x32_bf16 v[6:9], v[154:157], v[222:225], v[6:9]
	s_setprio 0
	s_add_i32 s70, s70, 2
	s_add_u32 s30, s30, 0x100
	s_addc_u32 s31, s31, 0
	s_add_u32 s68, s68, 0x100
	s_addc_u32 s69, s69, 0
	s_cmp_gt_u32 s70, 13
	s_cbranch_scc0 .LBB0_287
.LBB0_290:
	v_mov_b32_e32 v133, v1
	v_mov_b32_e32 v132, v189
	s_lshl_b32 s22, s52, 8
	s_or_b32 s22, s22, s46
	s_lshl_b32 s14, s53, 8
	v_lshl_add_u32 v132, v132, 3, s22
	v_readlane_b32 s22, v254, 4
	s_add_i32 s14, s14, s45
	v_readlane_b32 s23, v254, 5
	v_add_u32_e32 v142, s14, v133
	v_ashrrev_i32_e32 v133, 31, v132
	v_mov_b64_e32 v[136:137], s[22:23]
	s_movk_i32 s14, 0x1a00
	v_mad_i64_i32 v[134:135], s[22:23], v142, s14, v[136:137]
	v_lshlrev_b64 v[138:139], 1, v[132:133]
	v_lshl_add_u64 v[140:141], v[134:135], 0, v[138:139]
	v_cvt_pk_bf16_f32 v132, v128, v129
	v_cvt_pk_bf16_f32 v133, v130, v131
	v_cvt_pk_bf16_f32 v134, v124, v125
	v_cvt_pk_bf16_f32 v135, v126, v127
	global_store_dwordx4 v[140:141], v[132:135], off
	s_andn2_b64 vcc, exec, s[4:5]
	s_mov_b64 s[4:5], -1
	v_cvt_pk_bf16_f32 v132, v96, v97
	v_cvt_pk_bf16_f32 v133, v98, v99
	v_cvt_pk_bf16_f32 v134, v92, v93
	v_cvt_pk_bf16_f32 v135, v94, v95
	global_store_dwordx4 v[140:141], v[132:135], off offset:256
	s_cmp_eq_u64 s[8:9], 0
	s_cbranch_scc1 .Lepi_nobar_g1
	s_barrier
.Lepi_nobar_g1:
	s_mov_b32 s58, 0x19b00000
	v_readlane_b32 s59, v255, 10
	v_add_u32_e32 v132, 16, v142
	v_mad_i64_i32 v[132:133], s[22:23], v132, s14, v[136:137]
	v_lshl_add_u64 v[140:141], v[132:133], 0, v[138:139]
	v_cvt_pk_bf16_f32 v132, v120, v121
	v_cvt_pk_bf16_f32 v133, v122, v123
	v_cvt_pk_bf16_f32 v134, v116, v117
	v_cvt_pk_bf16_f32 v135, v118, v119
	global_store_dwordx4 v[140:141], v[132:135], off
	s_mov_b32 s60, 0xff61b1e6
	s_mov_b32 s56, 0x3a800000
	v_cvt_pk_bf16_f32 v132, v88, v89
	v_cvt_pk_bf16_f32 v133, v90, v91
	v_cvt_pk_bf16_f32 v134, v84, v85
	v_cvt_pk_bf16_f32 v135, v86, v87
	global_store_dwordx4 v[140:141], v[132:135], off offset:256
	s_mov_b64 s[62:63], 0x800
	s_mov_b32 s64, 0x3b000000
	v_add_u32_e32 v132, 32, v142
	v_mad_i64_i32 v[132:133], s[22:23], v132, s14, v[136:137]
	v_lshl_add_u64 v[140:141], v[132:133], 0, v[138:139]
	v_cvt_pk_bf16_f32 v132, v112, v113
	v_cvt_pk_bf16_f32 v133, v114, v115
	v_cvt_pk_bf16_f32 v134, v108, v109
	v_cvt_pk_bf16_f32 v135, v110, v111
	global_store_dwordx4 v[140:141], v[132:135], off
	s_nop 1
	v_cvt_pk_bf16_f32 v132, v80, v81
	v_cvt_pk_bf16_f32 v133, v82, v83
	v_cvt_pk_bf16_f32 v134, v76, v77
	v_cvt_pk_bf16_f32 v135, v78, v79
	global_store_dwordx4 v[140:141], v[132:135], off offset:256
	s_nop 1
	v_add_u32_e32 v132, 48, v142
	v_mad_i64_i32 v[132:133], s[22:23], v132, s14, v[136:137]
	v_lshl_add_u64 v[140:141], v[132:133], 0, v[138:139]
	v_cvt_pk_bf16_f32 v132, v104, v105
	v_cvt_pk_bf16_f32 v133, v106, v107
	v_cvt_pk_bf16_f32 v134, v100, v101
	v_cvt_pk_bf16_f32 v135, v102, v103
	global_store_dwordx4 v[140:141], v[132:135], off
	s_nop 1
	v_cvt_pk_bf16_f32 v132, v72, v73
	v_cvt_pk_bf16_f32 v133, v74, v75
	v_cvt_pk_bf16_f32 v134, v68, v69
	v_cvt_pk_bf16_f32 v135, v70, v71
	global_store_dwordx4 v[140:141], v[132:135], off offset:256
	s_nop 1
	v_add_u32_e32 v132, 0x80, v142
	v_mad_i64_i32 v[132:133], s[22:23], v132, s14, v[136:137]
	v_lshl_add_u64 v[140:141], v[132:133], 0, v[138:139]
	v_cvt_pk_bf16_f32 v132, v64, v65
	v_cvt_pk_bf16_f32 v133, v66, v67
	v_cvt_pk_bf16_f32 v134, v60, v61
	v_cvt_pk_bf16_f32 v135, v62, v63
	global_store_dwordx4 v[140:141], v[132:135], off
	s_nop 1
	v_cvt_pk_bf16_f32 v132, v30, v31
	v_cvt_pk_bf16_f32 v133, v32, v33
	v_cvt_pk_bf16_f32 v134, v26, v27
	v_cvt_pk_bf16_f32 v135, v28, v29
	global_store_dwordx4 v[140:141], v[132:135], off offset:256
	s_nop 1
	v_add_u32_e32 v132, 0x90, v142
	v_mad_i64_i32 v[132:133], s[22:23], v132, s14, v[136:137]
	v_lshl_add_u64 v[140:141], v[132:133], 0, v[138:139]
	v_cvt_pk_bf16_f32 v132, v56, v57
	v_cvt_pk_bf16_f32 v133, v58, v59
	v_cvt_pk_bf16_f32 v134, v52, v53
	v_cvt_pk_bf16_f32 v135, v54, v55
	global_store_dwordx4 v[140:141], v[132:135], off
	s_nop 1
	v_cvt_pk_bf16_f32 v132, v22, v23
	v_cvt_pk_bf16_f32 v133, v24, v25
	v_cvt_pk_bf16_f32 v134, v18, v19
	v_cvt_pk_bf16_f32 v135, v20, v21
	global_store_dwordx4 v[140:141], v[132:135], off offset:256
	s_nop 1
	v_add_u32_e32 v132, 0xa0, v142
	v_mad_i64_i32 v[132:133], s[22:23], v132, s14, v[136:137]
	v_lshl_add_u64 v[140:141], v[132:133], 0, v[138:139]
	v_cvt_pk_bf16_f32 v132, v48, v49
	v_cvt_pk_bf16_f32 v133, v50, v51
	v_cvt_pk_bf16_f32 v134, v44, v45
	v_cvt_pk_bf16_f32 v135, v46, v47
	global_store_dwordx4 v[140:141], v[132:135], off
	s_nop 1
	v_cvt_pk_bf16_f32 v132, v14, v15
	v_cvt_pk_bf16_f32 v133, v16, v17
	v_cvt_pk_bf16_f32 v134, v10, v11
	v_cvt_pk_bf16_f32 v135, v12, v13
	global_store_dwordx4 v[140:141], v[132:135], off offset:256
	s_nop 1
	v_add_u32_e32 v132, 0xb0, v142
	v_mad_i64_i32 v[132:133], s[22:23], v132, s14, v[136:137]
	v_lshl_add_u64 v[136:137], v[132:133], 0, v[138:139]
	v_cvt_pk_bf16_f32 v132, v40, v41
	v_cvt_pk_bf16_f32 v133, v42, v43
	v_cvt_pk_bf16_f32 v134, v36, v37
	v_cvt_pk_bf16_f32 v135, v38, v39
	global_store_dwordx4 v[136:137], v[132:135], off
	s_nop 1
	v_cvt_pk_bf16_f32 v132, v6, v7
	v_cvt_pk_bf16_f32 v133, v8, v9
	v_cvt_pk_bf16_f32 v134, v2, v3
	v_cvt_pk_bf16_f32 v135, v4, v5
	global_store_dwordx4 v[136:137], v[132:135], off offset:256
	s_cbranch_vccnz .LBB0_283
	s_andn2_b64 vcc, exec, s[6:7]
	s_cbranch_vccnz .LBB0_282
	s_barrier
	s_branch .LBB0_282
